# v23 + nt on the B-operand (fp8 expert weight) LDS-DMA loads of P7/P8
# baseline (speedup 1.0000x reference)
; #define PG8_STAGE(bufoff, gbase, voff) do { _Pragma("unroll") for (int _i = 0; _i < 2; ++_i) \
;         __builtin_amdgcn_global_load_lds((const unsigned*)((const char*)(gbase) + (voff)[_i]), (LAS unsigned*)(lds + (bufoff) + ldsw + _i * 8192), 16, 0, 0); } while (0)
; #define PG8_WAIT_V(n) asm volatile("s_waitcnt vmcnt(" #n ")" ::: "memory")
; #define PG8_BAR __builtin_amdgcn_s_barrier()
; template <class Epi, class Sched, bool GATHER, bool F8 = false>
; __device__ __forceinline__ void gemm_phase(LAS unsigned char* lds, const int K, const Sched& S, const Epi& E) {
;     ...
;     if constexpr (EpiInit<Epi>::value) { const typename EpiInit<Epi>::Pre p0 = E.preload(cur, wr, wc, fr, fq); E.init(acc, p0); }
;     int one_scale = 0x7f7f7f7f; asm volatile("" : "+v"(one_scale));
;     bf16x8 At[4][2], B0[2][2], B1[2][2]; i32x8 At8[4], B08[2], B18[2];
;     const char* cA = cur.A; const char* cB = cur.B;
;     PG8_STAGE(PG8_SB(0, 0), cB, voffB); PG8_STAGE(PG8_SB(0, 1), cB + hstepB, voffB); PG8_STAGE(PG8_SA(0, 0), cA, vA[0]); PG8_STAGE(PG8_SA(0, 1), cA, vA[1]);
;     if (wr == 1) PG8_BAR;
;     PG8_WAIT_V(2); PG8_BAR;
;     PG8_STAGE(PG8_SB(1, 0), cB + kstep, voffB); PG8_STAGE(PG8_SA(1, 0), cA + kstep, vA[0]); PG8_STAGE(PG8_SB(1, 1), cB + hstepB + kstep, voffB);
;     PG8_WAIT_V(6); PG8_BAR;
; __global__ void __launch_bounds__(512, 2) fwd(Args args) {
;     ...
;           for (int k = 0; k < 5; ++k) { Unit u; toks[k] = 0;
;               if (S.next(2 * k + ih, u)) { const int tile = u.row0 >> 8, e = u.tag, r0 = tab[160 + tile] * 256, n = tab[320 + e]; if (r0 + r < n) toks[k] = tokl[e * NTOK + r0 + r]; } }
; #pragma unroll
;           for (int k = 0; k < 5; ++k) tab[512 + (2 * k + ih) * 256 + r] = toks[k];
;           __syncthreads(); }
.LBB0_1027:
	s_or_b64 exec, exec, s[10:11]
	v_and_b32_e32 v2, 0x100, v0
	v_mov_b32_e32 v5, 2
	s_add_i32 s0, 0, 0x20000
	v_lshlrev_b32_e32 v2, 2, v2
	v_lshlrev_b32_sdwa v5, v5, v0 dst_sel:DWORD dst_unused:UNUSED_PAD src0_sel:DWORD src1_sel:BYTE_0
	s_or_b32 s6, s6, s7
	v_add3_u32 v2, s0, v2, v5
	s_cmp_ge_i32 s6, s3
	v_readfirstlane_b32 s20, v0
	s_waitcnt vmcnt(0)
	ds_write2st64_b32 v2, v4, v1 offset0:8 offset1:16
	ds_write2st64_b32 v2, v7, v6 offset0:24 offset1:32
	ds_write_b32 v2, v3 offset:10240
	s_waitcnt lgkmcnt(0)
	s_barrier
	s_cbranch_scc1 .LBB0_1045
	v_lshlrev_b32_e32 v1, 4, v0
	v_and_b32_e32 v2, 32, v0
	v_bfe_u32 v4, v0, 3, 25
	s_add_u32 s7, s82, 0x4000000
	v_bfe_u32 v3, v0, 2, 4
	v_bitop3_b32 v1, v1, v2, 48 bitop3:0x6c
	v_lshrrev_b32_e32 v2, 3, v0
	v_or_b32_e32 v4, 64, v4
	s_movk_i32 s0, 0x70
	s_addc_u32 s25, s83, 0
	v_and_or_b32 v160, v2, 48, v3
	v_and_or_b32 v161, v4, s0, v3
	s_lshl_b32 s0, s20, 4
	v_lshrrev_b32_e32 v3, 1, v0
	s_and_b32 s37, s0, 0xfffffc00
	v_and_b32_e32 v14, 24, v3
	s_lshr_b32 s0, s20, 1
	v_lshrrev_b32_e32 v3, 5, v0
	s_lshr_b32 s21, s20, 8
	s_and_b32 s14, s0, 0x60
	v_and_b32_e32 v3, 4, v3
	v_bfe_u32 v5, v0, 2, 2
	s_movk_i32 s10, 0x60
	s_add_u32 s0, s82, 0x2c000000
	v_or3_b32 v3, v3, v5, v14
	s_addc_u32 s1, s83, 0
	v_and_or_b32 v4, v4, s10, v3
	s_lshl_b32 s10, s6, 2
	s_add_i32 s10, s10, 0
	v_and_or_b32 v1, v0, 64, v1
	v_and_or_b32 v2, v2, 32, v3
	s_add_i32 s10, s10, 0x20000
	v_lshl_or_b32 v148, v2, 11, v1
	v_mov_b32_e32 v2, s10
	ds_read_b32 v150, v2
	s_lshl_b32 s10, s2, 3
	s_and_b32 s39, s10, 8
	s_ashr_i32 s10, s2, 5
	s_add_i32 s39, s39, s10
	s_waitcnt lgkmcnt(0)
	v_readfirstlane_b32 s10, v150
	s_lshl_b32 s10, s10, 4
	s_add_i32 s10, s10, s39
	s_ashr_i32 s11, s10, 31
	s_lshl_b64 s[10:11], s[10:11], 19
	s_add_u32 s44, s7, s10
	v_lshl_or_b32 v146, v4, 11, v1
	v_bfe_u32 v254, v148, 11, 5
	v_and_b32_e32 v148, 0xffff007f, v148
	v_lshl_or_b32 v148, v254, 7, v148
	v_bfe_u32 v254, v146, 11, 5
	v_and_b32_e32 v146, 0xffff007f, v146
	v_lshl_or_b32 v146, v254, 7, v146
	s_addc_u32 s45, s25, s11
	s_add_i32 s10, 0, 0x20800
	v_lshlrev_b32_e32 v2, 2, v160
	v_lshlrev_b32_e32 v4, 2, v161
	v_add_u32_e32 v3, s10, v2
	v_add_u32_e32 v5, s10, v4
	s_add_i32 s10, 0, 0x20a00
	v_add_u32_e32 v2, s10, v2
	v_add_u32_e32 v4, s10, v4
	ds_read_b32 v3, v3
	ds_read_b32 v5, v5
	ds_read_b32 v2, v2
	ds_read_b32 v4, v4
	s_lshl_b32 s50, s39, 7
	v_or_b32_e32 v162, s14, v14
	v_ashrrev_i32_e32 v151, 31, v150
	s_waitcnt lgkmcnt(1)
	v_lshl_or_b32 v163, v2, 11, v1
	v_or_b32_e32 v2, s50, v162
	v_lshl_or_b32 v152, v3, 11, v1
	v_lshl_or_b32 v154, v5, 11, v1
	s_waitcnt lgkmcnt(0)
	v_lshl_or_b32 v164, v4, 11, v1
	v_lshlrev_b64 v[4:5], 13, v[150:151]
	v_ashrrev_i32_e32 v3, 31, v2
	v_lshl_add_u64 v[6:7], s[18:19], 0, v[4:5]
	v_lshlrev_b64 v[2:3], 2, v[2:3]
	s_add_i32 s51, s37, 0
	v_lshl_add_u64 v[10:11], v[6:7], 0, v[2:3]
	v_lshl_add_u64 v[4:5], s[22:23], 0, v[4:5]
	v_mov_b32_e32 v165, 0x7f7f7f7f
	s_add_i32 m0, s51, 0x10000
	v_lshl_add_u64 v[12:13], v[4:5], 0, v[2:3]
	global_load_dwordx4 v[58:61], v[10:11], off offset:16
	global_load_dwordx4 v[62:65], v[10:11], off
	global_load_dwordx4 v[2:5], v[12:13], off offset:16
	global_load_dwordx4 v[6:9], v[12:13], off
	global_load_lds_dwordx4 v148, s[44:45] nt
	s_add_i32 m0, s51, 0x12000
	s_add_u32 s10, s44, 0x40000
	global_load_lds_dwordx4 v146, s[44:45] nt
	s_addc_u32 s11, s45, 0
	s_add_i32 m0, s51, 0x14000
	s_add_i32 s52, s51, 0x2000
	global_load_lds_dwordx4 v148, s[10:11] nt
	s_add_i32 m0, s51, 0x16000
	s_add_i32 s53, s51, 0x4000
	global_load_lds_dwordx4 v146, s[10:11] nt
	s_mov_b32 m0, s51
	s_add_i32 s54, s51, 0x6000
	global_load_lds_dwordx4 v152, s[0:1]
	s_mov_b32 m0, s52
	v_mov_b32_e32 v153, 0
	global_load_lds_dwordx4 v154, s[0:1]
	s_mov_b32 m0, s53
	v_mov_b32_e32 v149, v153
	global_load_lds_dwordx4 v163, s[0:1]
	s_mov_b32 m0, s54
	v_mov_b32_e32 v147, v153
	global_load_lds_dwordx4 v164, s[0:1]
	s_cmp_eq_u32 s21, 1
	v_lshl_add_u64 v[12:13], s[44:45], 0, v[148:149]
	v_lshl_add_u64 v[10:11], s[44:45], 0, v[146:147]
	s_cselect_b64 s[10:11], -1, 0
	s_cmp_lg_u32 s21, 1
	v_mov_b32_e32 v155, v153
	s_cbranch_scc1 .LBB0_1030
	s_barrier
.LBB0_1030:
	s_lshl_b32 s64, s6, 8
	s_add_u32 s12, s82, 0x34000000
	s_addc_u32 s13, s83, 0
	s_lshl_b32 s36, s14, 7
	s_mov_b64 s[14:15], 0x80
	s_mov_b64 s[100:101], 0x1000
	s_add_i32 m0, s51, 0x18000
	v_lshl_add_u64 v[12:13], v[12:13], 0, s[100:101]
	s_lshl_b32 s24, s21, 13
	s_waitcnt vmcnt(2)
	s_barrier
	global_load_lds_dwordx4 v[12:13], off nt
	s_add_i32 m0, s51, 0x1a000
	s_add_u32 s16, s82, 0x2c000080
	v_lshl_add_u64 v[10:11], v[10:11], 0, s[100:101]
	s_addc_u32 s17, s83, 0
	s_add_i32 s55, s51, 0x8000
	s_add_i32 s56, s51, 0xa000
	global_load_lds_dwordx4 v[10:11], off nt
	v_lshl_add_u64 v[10:11], s[16:17], 0, v[152:153]
	s_mov_b32 m0, s55
	s_add_u32 s40, s44, 0x41000
	global_load_lds_dwordx4 v[10:11], off
	v_lshl_add_u64 v[10:11], s[16:17], 0, v[154:155]
	s_mov_b32 m0, s56
	s_addc_u32 s41, s45, 0
	global_load_lds_dwordx4 v[10:11], off
	s_add_i32 m0, s51, 0x1c000
	v_lshl_add_u64 v[10:11], s[40:41], 0, v[148:149]
	global_load_lds_dwordx4 v[10:11], off nt
	v_lshl_add_u64 v[10:11], s[40:41], 0, v[146:147]
	s_add_i32 m0, s51, 0x1e000
	v_lshlrev_b32_e32 v12, 2, v0
	global_load_lds_dwordx4 v[10:11], off nt
	v_and_b32_e32 v10, 15, v0
	v_lshlrev_b32_e32 v11, 1, v14
	v_lshl_or_b32 v166, s21, 6, v10
	v_lshl_or_b32 v10, v10, 6, v11
	v_and_b32_e32 v12, 32, v12
	v_lshlrev_b32_e32 v13, 6, v0
	s_movk_i32 s21, 0x3c0
	s_waitcnt vmcnt(6)
	v_bitop3_b32 v10, v10, s24, v12 bitop3:0xde
	v_and_or_b32 v11, v13, s21, v11
	s_cmpk_lt_u32 s20, 0x100
	v_bitop3_b32 v167, s36, v11, v12 bitop3:0xf6
	s_mov_b32 s57, 0
	s_cselect_b64 s[20:21], -1, 0
	s_mov_b32 s24, 0x42800000
	s_add_i32 s58, 0, 0x10000
	s_add_i32 s59, 0, 0x14000
	v_add_u32_e32 v168, 0, v10
	s_mov_b32 s36, 0x3c800000
	s_mov_b32 s60, 0xc0c00000
	s_mov_b32 s38, 0xc01d265f
	s_add_i32 s61, s51, 0xc000
	s_add_i32 s62, s51, 0xe000
	v_mov_b32_e32 v169, 0x41000000
	s_mov_b64 s[40:41], s[44:45]
	s_barrier
	s_branch .LBB0_1033

; #define PG8_STAGE(bufoff, gbase, voff) do { _Pragma("unroll") for (int _i = 0; _i < 2; ++_i) \
;         __builtin_amdgcn_global_load_lds((const unsigned*)((const char*)(gbase) + (voff)[_i]), (LAS unsigned*)(lds + (bufoff) + ldsw + _i * 8192), 16, 0, 0); } while (0)
; #define PG8_LDA(dst, b, h) do { _Pragma("unroll") for (int m = 0; m < 4; ++m) { if constexpr (F8) dst##8[m] = PG8_LD32(lds + PG8_SA(b, h) + aoff + m * 2048); \
;         else { _Pragma("unroll") for (int k = 0; k < 2; ++k) dst[m][k] = *(const LAS bf16x8*)(lds + PG8_SA(b, h) + aoff + m * 2048 + k * 1024); } } } while (0)
; #define PG8_LDB(dst, b, h) do { _Pragma("unroll") for (int n = 0; n < 2; ++n) { if constexpr (F8) dst##8[n] = PG8_LD32(lds + PG8_SB(b, h) + boff + n * 2048); \
;         else { _Pragma("unroll") for (int k = 0; k < 2; ++k) dst[n][k] = *(const LAS bf16x8*)(lds + PG8_SB(b, h) + boff + n * 2048 + k * 1024); } } } while (0)
; #define PG8_WAIT_V(n) asm volatile("s_waitcnt vmcnt(" #n ")" ::: "memory")
; #define PG8_WAIT_L(n) asm volatile("s_waitcnt lgkmcnt(" #n ")" ::: "memory")
; #define PG8_BAR __builtin_amdgcn_s_barrier()
; #define PG8_SCHED __builtin_amdgcn_sched_barrier(0)
; template <class Epi, class Sched, bool GATHER, bool F8 = false>
; __device__ __forceinline__ void gemm_phase(LAS unsigned char* lds, const int K, const Sched& S, const Epi& E) {
;     ...
;             PG8_LDB(B0, 0, 0); PG8_LDB(B1, 0, 1); PG8_SCHED; PG8_LDA(At, 0, 0); PG8_STAGE(PG8_SA(1, 1), a1, vA[1]);
;             PG8_WAIT_V(8); PG8_WAIT_L(0); PG8_BAR; PG8_MMA(0, 0, At, B0); PG8_MMA(0, 1, At, B1); PG8_BAR; PG8_SCHED;
;             PG8_LDA(At, 0, 1); PG8_STAGE(PG8_SB(0, 0), b2, voffB); PG8_STAGE(PG8_SB(0, 1), b2 + hstepB, voffB); PG8_STAGE(PG8_SA(0, 0), a2, vN[0]);
;             PG8_WAIT_V(8); PG8_WAIT_L(0); PG8_BAR; PG8_MMA(1, 0, At, B0); PG8_MMA(1, 1, At, B1); PG8_BAR; PG8_SCHED;
.LBB0_1036:
	v_add_u32_e32 v62, s58, v167
	ds_read_b128 v[2:5], v62
	ds_read_b128 v[6:9], v62 offset:1024
	ds_read_b128 v[172:175], v62 offset:2048
	ds_read_b128 v[176:179], v62 offset:3072
	v_add_u32_e32 v62, s59, v167
	ds_read_b128 v[180:183], v62
	ds_read_b128 v[184:187], v62 offset:1024
	ds_read_b128 v[188:191], v62 offset:2048
	ds_read_b128 v[192:195], v62 offset:3072
	s_add_u32 s48, s44, 0x80
	s_addc_u32 s49, s45, 0
	s_and_b64 s[46:47], s[46:47], exec
	s_cselect_b32 s49, s1, s49
	s_cselect_b32 s48, s0, s48
	s_cselect_b32 s47, s41, s66
	s_cselect_b32 s46, s40, s65
	s_mov_b32 m0, s61
	v_lshl_add_u64 v[62:63], s[44:45], 0, v[58:59]
	ds_read_b128 v[196:199], v168
	ds_read_b128 v[200:203], v168 offset:1024
	ds_read_b128 v[204:207], v168 offset:2048
	ds_read_b128 v[208:211], v168 offset:3072
	ds_read_b128 v[212:215], v168 offset:4096
	ds_read_b128 v[216:219], v168 offset:5120
	ds_read_b128 v[220:223], v168 offset:6144
	ds_read_b128 v[224:227], v168 offset:7168
	global_load_lds_dwordx4 v[62:63], off
	v_lshl_add_u64 v[62:63], s[44:45], 0, v[60:61]
	s_mov_b32 m0, s62
	s_nop 0
	global_load_lds_dwordx4 v[62:63], off
	s_waitcnt vmcnt(8)
	s_waitcnt lgkmcnt(0)
	s_barrier
	s_setprio 1
	s_waitcnt lgkmcnt(0)
	v_mfma_scale_f32_16x16x128_f8f6f4 v[142:145], v[2:9], v[196:203], v[142:145], v165, v165 op_sel_hi:[0,0,0]
	v_mfma_scale_f32_16x16x128_f8f6f4 v[134:137], v[172:179], v[196:203], v[134:137], v165, v165 op_sel_hi:[0,0,0]
	v_mfma_scale_f32_16x16x128_f8f6f4 v[126:129], v[2:9], v[204:211], v[126:129], v165, v165 op_sel_hi:[0,0,0]
	v_mfma_scale_f32_16x16x128_f8f6f4 v[118:121], v[172:179], v[204:211], v[118:121], v165, v165 op_sel_hi:[0,0,0]
	v_mfma_scale_f32_16x16x128_f8f6f4 v[110:113], v[2:9], v[212:219], v[110:113], v165, v165 op_sel_hi:[0,0,0]
	v_mfma_scale_f32_16x16x128_f8f6f4 v[102:105], v[172:179], v[212:219], v[102:105], v165, v165 op_sel_hi:[0,0,0]
	v_mfma_scale_f32_16x16x128_f8f6f4 v[94:97], v[2:9], v[220:227], v[94:97], v165, v165 op_sel_hi:[0,0,0]
	v_mfma_scale_f32_16x16x128_f8f6f4 v[86:89], v[172:179], v[220:227], v[86:89], v165, v165 op_sel_hi:[0,0,0]
	s_setprio 0
	s_setprio 1
	v_mfma_scale_f32_16x16x128_f8f6f4 v[138:141], v[180:187], v[196:203], v[138:141], v165, v165 op_sel_hi:[0,0,0]
	v_mfma_scale_f32_16x16x128_f8f6f4 v[130:133], v[188:195], v[196:203], v[130:133], v165, v165 op_sel_hi:[0,0,0]
	v_mfma_scale_f32_16x16x128_f8f6f4 v[122:125], v[180:187], v[204:211], v[122:125], v165, v165 op_sel_hi:[0,0,0]
	v_mfma_scale_f32_16x16x128_f8f6f4 v[114:117], v[188:195], v[204:211], v[114:117], v165, v165 op_sel_hi:[0,0,0]
	v_mfma_scale_f32_16x16x128_f8f6f4 v[106:109], v[180:187], v[212:219], v[106:109], v165, v165 op_sel_hi:[0,0,0]
	v_mfma_scale_f32_16x16x128_f8f6f4 v[98:101], v[188:195], v[212:219], v[98:101], v165, v165 op_sel_hi:[0,0,0]
	v_mfma_scale_f32_16x16x128_f8f6f4 v[90:93], v[180:187], v[220:227], v[90:93], v165, v165 op_sel_hi:[0,0,0]
	v_mfma_scale_f32_16x16x128_f8f6f4 v[82:85], v[188:195], v[220:227], v[82:85], v165, v165 op_sel_hi:[0,0,0]
	s_setprio 0
	s_barrier
	s_add_i32 s68, s58, s37
	v_lshl_add_u64 v[62:63], s[46:47], 0, v[148:149]
	s_mov_b32 m0, s68
	ds_read_b128 v[196:199], v168 offset:16384
	ds_read_b128 v[200:203], v168 offset:17408
	ds_read_b128 v[204:207], v168 offset:18432
	ds_read_b128 v[208:211], v168 offset:19456
	ds_read_b128 v[212:215], v168 offset:20480
	ds_read_b128 v[216:219], v168 offset:21504
	ds_read_b128 v[220:223], v168 offset:22528
	ds_read_b128 v[224:227], v168 offset:23552
	global_load_lds_dwordx4 v[62:63], off nt
	s_add_i32 m0, s68, 0x2000
	s_add_u32 s68, s46, 0x40000
	v_lshl_add_u64 v[64:65], s[46:47], 0, v[146:147]
	s_addc_u32 s69, s47, 0
	s_add_i32 s70, s59, s37
	global_load_lds_dwordx4 v[64:65], off nt
	v_lshl_add_u64 v[156:157], s[68:69], 0, v[148:149]
	s_mov_b32 m0, s70
	v_mov_b32_e32 v155, v153
	global_load_lds_dwordx4 v[156:157], off nt
	v_lshl_add_u64 v[156:157], s[68:69], 0, v[146:147]
	s_add_i32 m0, s70, 0x2000
	v_lshl_add_u64 v[158:159], s[48:49], 0, v[152:153]
	global_load_lds_dwordx4 v[156:157], off nt
	s_mov_b32 m0, s51
	v_lshl_add_u64 v[156:157], s[48:49], 0, v[154:155]
	global_load_lds_dwordx4 v152, s[48:49]
	s_mov_b32 m0, s52
	s_nop 0
	global_load_lds_dwordx4 v154, s[48:49]
	s_waitcnt vmcnt(8)
	s_waitcnt lgkmcnt(0)
	s_barrier
	s_setprio 1
	s_waitcnt lgkmcnt(0)
	v_mfma_scale_f32_16x16x128_f8f6f4 v[78:81], v[2:9], v[196:203], v[78:81], v165, v165 op_sel_hi:[0,0,0]
	v_mfma_scale_f32_16x16x128_f8f6f4 v[70:73], v[172:179], v[196:203], v[70:73], v165, v165 op_sel_hi:[0,0,0]
	v_mfma_scale_f32_16x16x128_f8f6f4 v[54:57], v[2:9], v[204:211], v[54:57], v165, v165 op_sel_hi:[0,0,0]
	v_mfma_scale_f32_16x16x128_f8f6f4 v[46:49], v[172:179], v[204:211], v[46:49], v165, v165 op_sel_hi:[0,0,0]
	v_mfma_scale_f32_16x16x128_f8f6f4 v[38:41], v[2:9], v[212:219], v[38:41], v165, v165 op_sel_hi:[0,0,0]
	v_mfma_scale_f32_16x16x128_f8f6f4 v[30:33], v[172:179], v[212:219], v[30:33], v165, v165 op_sel_hi:[0,0,0]
	v_mfma_scale_f32_16x16x128_f8f6f4 v[18:21], v[2:9], v[220:227], v[18:21], v165, v165 op_sel_hi:[0,0,0]
	v_mfma_scale_f32_16x16x128_f8f6f4 v[10:13], v[172:179], v[220:227], v[10:13], v165, v165 op_sel_hi:[0,0,0]
	s_setprio 0
	s_setprio 1
	v_mfma_scale_f32_16x16x128_f8f6f4 v[74:77], v[180:187], v[196:203], v[74:77], v165, v165 op_sel_hi:[0,0,0]
	v_mfma_scale_f32_16x16x128_f8f6f4 v[66:69], v[188:195], v[196:203], v[66:69], v165, v165 op_sel_hi:[0,0,0]
	v_mfma_scale_f32_16x16x128_f8f6f4 v[50:53], v[180:187], v[204:211], v[50:53], v165, v165 op_sel_hi:[0,0,0]
	v_mfma_scale_f32_16x16x128_f8f6f4 v[42:45], v[188:195], v[204:211], v[42:45], v165, v165 op_sel_hi:[0,0,0]
	v_mfma_scale_f32_16x16x128_f8f6f4 v[34:37], v[180:187], v[212:219], v[34:37], v165, v165 op_sel_hi:[0,0,0]
	v_mfma_scale_f32_16x16x128_f8f6f4 v[26:29], v[188:195], v[212:219], v[26:29], v165, v165 op_sel_hi:[0,0,0]
	v_mfma_scale_f32_16x16x128_f8f6f4 v[22:25], v[180:187], v[220:227], v[22:25], v165, v165 op_sel_hi:[0,0,0]
	v_mfma_scale_f32_16x16x128_f8f6f4 v[14:17], v[188:195], v[220:227], v[14:17], v165, v165 op_sel_hi:[0,0,0]
	s_setprio 0
	s_barrier
; #define PG8_STAGE(bufoff, gbase, voff) do { _Pragma("unroll") for (int _i = 0; _i < 2; ++_i) \
;         __builtin_amdgcn_global_load_lds((const unsigned*)((const char*)(gbase) + (voff)[_i]), (LAS unsigned*)(lds + (bufoff) + ldsw + _i * 8192), 16, 0, 0); } while (0)
; #define PG8_LDA(dst, b, h) do { _Pragma("unroll") for (int m = 0; m < 4; ++m) { if constexpr (F8) dst##8[m] = PG8_LD32(lds + PG8_SA(b, h) + aoff + m * 2048); \
;         else { _Pragma("unroll") for (int k = 0; k < 2; ++k) dst[m][k] = *(const LAS bf16x8*)(lds + PG8_SA(b, h) + aoff + m * 2048 + k * 1024); } } } while (0)
; #define PG8_LDB(dst, b, h) do { _Pragma("unroll") for (int n = 0; n < 2; ++n) { if constexpr (F8) dst##8[n] = PG8_LD32(lds + PG8_SB(b, h) + boff + n * 2048); \
;         else { _Pragma("unroll") for (int k = 0; k < 2; ++k) dst[n][k] = *(const LAS bf16x8*)(lds + PG8_SB(b, h) + boff + n * 2048 + k * 1024); } } } while (0)
; #define PG8_WAIT_V(n) asm volatile("s_waitcnt vmcnt(" #n ")" ::: "memory")
; #define PG8_WAIT_L(n) asm volatile("s_waitcnt lgkmcnt(" #n ")" ::: "memory")
; #define PG8_BAR __builtin_amdgcn_s_barrier()
; #define PG8_SCHED __builtin_amdgcn_sched_barrier(0)
; template <class Epi, class Sched, bool GATHER, bool F8 = false>
; __device__ __forceinline__ void gemm_phase(LAS unsigned char* lds, const int K, const Sched& S, const Epi& E) {
;     ...
;             PG8_LDB(B0, 1, 0); PG8_LDB(B1, 1, 1); PG8_SCHED; PG8_LDA(At, 1, 0); PG8_STAGE(PG8_SA(0, 1), a2, vN[1]);
;             PG8_WAIT_V(8); PG8_WAIT_L(0); PG8_BAR; PG8_MMA(0, 0, At, B0); PG8_MMA(0, 1, At, B1); PG8_BAR; PG8_SCHED;
;             PG8_LDA(At, 1, 1); PG8_STAGE(PG8_SB(1, 0), b3, voffB); PG8_STAGE(PG8_SB(1, 1), b3 + hstepB, voffB); PG8_STAGE(PG8_SA(1, 0), a3, vN[0]);
;             PG8_WAIT_V(8); PG8_WAIT_L(0); PG8_BAR; PG8_MMA(1, 0, At, B0); PG8_MMA(1, 1, At, B1); PG8_BAR; PG8_SCHED;
;         }
	s_add_i32 s68, 0, 0x18000
	s_add_i32 s69, 0, 0x1c000
	v_add_u32_e32 v2, s68, v167
	v_add_u32_e32 v155, s69, v167
	ds_read_b128 v[172:175], v2
	ds_read_b128 v[176:179], v2 offset:1024
	ds_read_b128 v[180:183], v2 offset:2048
	ds_read_b128 v[184:187], v2 offset:3072
	ds_read_b128 v[2:5], v155
	ds_read_b128 v[6:9], v155 offset:1024
	ds_read_b128 v[188:191], v155 offset:2048
	ds_read_b128 v[192:195], v155 offset:3072
	s_mov_b32 m0, s53
	ds_read_b128 v[196:199], v168 offset:32768
	ds_read_b128 v[200:203], v168 offset:33792
	ds_read_b128 v[204:207], v168 offset:34816
	ds_read_b128 v[208:211], v168 offset:35840
	ds_read_b128 v[212:215], v168 offset:36864
	ds_read_b128 v[216:219], v168 offset:37888
	ds_read_b128 v[220:223], v168 offset:38912
	ds_read_b128 v[224:227], v168 offset:39936
	global_load_lds_dwordx4 v163, s[48:49]
	s_mov_b32 m0, s54
	s_nop 0
	global_load_lds_dwordx4 v164, s[48:49]
	s_waitcnt vmcnt(8)
	s_waitcnt lgkmcnt(0)
	s_barrier
	s_setprio 1
	s_waitcnt lgkmcnt(0)
	v_mfma_scale_f32_16x16x128_f8f6f4 v[142:145], v[172:179], v[196:203], v[142:145], v165, v165 op_sel_hi:[0,0,0]
	v_mfma_scale_f32_16x16x128_f8f6f4 v[134:137], v[180:187], v[196:203], v[134:137], v165, v165 op_sel_hi:[0,0,0]
	v_mfma_scale_f32_16x16x128_f8f6f4 v[126:129], v[172:179], v[204:211], v[126:129], v165, v165 op_sel_hi:[0,0,0]
	v_mfma_scale_f32_16x16x128_f8f6f4 v[118:121], v[180:187], v[204:211], v[118:121], v165, v165 op_sel_hi:[0,0,0]
	v_mfma_scale_f32_16x16x128_f8f6f4 v[110:113], v[172:179], v[212:219], v[110:113], v165, v165 op_sel_hi:[0,0,0]
	v_mfma_scale_f32_16x16x128_f8f6f4 v[102:105], v[180:187], v[212:219], v[102:105], v165, v165 op_sel_hi:[0,0,0]
	v_mfma_scale_f32_16x16x128_f8f6f4 v[94:97], v[172:179], v[220:227], v[94:97], v165, v165 op_sel_hi:[0,0,0]
	v_mfma_scale_f32_16x16x128_f8f6f4 v[86:89], v[180:187], v[220:227], v[86:89], v165, v165 op_sel_hi:[0,0,0]
	s_setprio 0
	s_setprio 1
	v_mfma_scale_f32_16x16x128_f8f6f4 v[138:141], v[2:9], v[196:203], v[138:141], v165, v165 op_sel_hi:[0,0,0]
	v_mfma_scale_f32_16x16x128_f8f6f4 v[130:133], v[188:195], v[196:203], v[130:133], v165, v165 op_sel_hi:[0,0,0]
	v_mfma_scale_f32_16x16x128_f8f6f4 v[122:125], v[2:9], v[204:211], v[122:125], v165, v165 op_sel_hi:[0,0,0]
	v_mfma_scale_f32_16x16x128_f8f6f4 v[114:117], v[188:195], v[204:211], v[114:117], v165, v165 op_sel_hi:[0,0,0]
	v_mfma_scale_f32_16x16x128_f8f6f4 v[106:109], v[2:9], v[212:219], v[106:109], v165, v165 op_sel_hi:[0,0,0]
	v_mfma_scale_f32_16x16x128_f8f6f4 v[98:101], v[188:195], v[212:219], v[98:101], v165, v165 op_sel_hi:[0,0,0]
	v_mfma_scale_f32_16x16x128_f8f6f4 v[90:93], v[2:9], v[220:227], v[90:93], v165, v165 op_sel_hi:[0,0,0]
	v_mfma_scale_f32_16x16x128_f8f6f4 v[82:85], v[188:195], v[220:227], v[82:85], v165, v165 op_sel_hi:[0,0,0]
	s_setprio 0
	s_barrier
	s_add_i32 s48, s68, s37
	v_lshl_add_u64 v[62:63], v[62:63], 0, s[100:101]
	s_mov_b32 m0, s48
	ds_read_b128 v[196:199], v168 offset:49152
	ds_read_b128 v[200:203], v168 offset:50176
	ds_read_b128 v[204:207], v168 offset:51200
	ds_read_b128 v[208:211], v168 offset:52224
	ds_read_b128 v[212:215], v168 offset:53248
	ds_read_b128 v[216:219], v168 offset:54272
	ds_read_b128 v[220:223], v168 offset:55296
	ds_read_b128 v[224:227], v168 offset:56320
	global_load_lds_dwordx4 v[62:63], off nt
	s_add_i32 m0, s48, 0x2000
	s_add_u32 s46, s46, 0x41000
	v_lshl_add_u64 v[62:63], v[64:65], 0, s[100:101]
	s_addc_u32 s47, s47, 0
	s_add_i32 s48, s69, s37
	global_load_lds_dwordx4 v[62:63], off nt
	v_lshl_add_u64 v[62:63], s[46:47], 0, v[148:149]
	s_mov_b32 m0, s48
	s_nop 0
	global_load_lds_dwordx4 v[62:63], off nt
	v_lshl_add_u64 v[62:63], s[46:47], 0, v[146:147]
	s_add_i32 m0, s48, 0x2000
	s_nop 0
	global_load_lds_dwordx4 v[62:63], off nt
	v_lshl_add_u64 v[62:63], v[158:159], 0, s[14:15]
	s_mov_b32 m0, s55
	s_nop 0
	global_load_lds_dwordx4 v[62:63], off
	v_lshl_add_u64 v[62:63], v[156:157], 0, s[14:15]
	s_mov_b32 m0, s56
	s_nop 0
	global_load_lds_dwordx4 v[62:63], off
	s_waitcnt vmcnt(8)
	s_waitcnt lgkmcnt(0)
	s_barrier
	s_setprio 1
	s_waitcnt lgkmcnt(0)
	v_mfma_scale_f32_16x16x128_f8f6f4 v[78:81], v[172:179], v[196:203], v[78:81], v165, v165 op_sel_hi:[0,0,0]
	v_mfma_scale_f32_16x16x128_f8f6f4 v[70:73], v[180:187], v[196:203], v[70:73], v165, v165 op_sel_hi:[0,0,0]
	v_mfma_scale_f32_16x16x128_f8f6f4 v[54:57], v[172:179], v[204:211], v[54:57], v165, v165 op_sel_hi:[0,0,0]
	v_mfma_scale_f32_16x16x128_f8f6f4 v[46:49], v[180:187], v[204:211], v[46:49], v165, v165 op_sel_hi:[0,0,0]
	v_mfma_scale_f32_16x16x128_f8f6f4 v[38:41], v[172:179], v[212:219], v[38:41], v165, v165 op_sel_hi:[0,0,0]
	v_mfma_scale_f32_16x16x128_f8f6f4 v[30:33], v[180:187], v[212:219], v[30:33], v165, v165 op_sel_hi:[0,0,0]
	v_mfma_scale_f32_16x16x128_f8f6f4 v[18:21], v[172:179], v[220:227], v[18:21], v165, v165 op_sel_hi:[0,0,0]
	v_mfma_scale_f32_16x16x128_f8f6f4 v[10:13], v[180:187], v[220:227], v[10:13], v165, v165 op_sel_hi:[0,0,0]
	s_setprio 0
	s_setprio 1
	v_mfma_scale_f32_16x16x128_f8f6f4 v[74:77], v[2:9], v[196:203], v[74:77], v165, v165 op_sel_hi:[0,0,0]
	v_mfma_scale_f32_16x16x128_f8f6f4 v[66:69], v[188:195], v[196:203], v[66:69], v165, v165 op_sel_hi:[0,0,0]
	v_mfma_scale_f32_16x16x128_f8f6f4 v[50:53], v[2:9], v[204:211], v[50:53], v165, v165 op_sel_hi:[0,0,0]
	v_mfma_scale_f32_16x16x128_f8f6f4 v[42:45], v[188:195], v[204:211], v[42:45], v165, v165 op_sel_hi:[0,0,0]
	v_mfma_scale_f32_16x16x128_f8f6f4 v[34:37], v[2:9], v[212:219], v[34:37], v165, v165 op_sel_hi:[0,0,0]
	v_mfma_scale_f32_16x16x128_f8f6f4 v[26:29], v[188:195], v[212:219], v[26:29], v165, v165 op_sel_hi:[0,0,0]
	v_mfma_scale_f32_16x16x128_f8f6f4 v[22:25], v[2:9], v[220:227], v[22:25], v165, v165 op_sel_hi:[0,0,0]
	v_mfma_scale_f32_16x16x128_f8f6f4 v[14:17], v[188:195], v[220:227], v[14:17], v165, v165 op_sel_hi:[0,0,0]
	s_setprio 0
	s_barrier
	s_add_i32 s67, s67, 2
	s_add_u32 s44, s44, 0x100
	s_addc_u32 s45, s45, 0
	s_add_u32 s65, s65, 0x2000
	s_addc_u32 s66, s66, 0
	s_cmp_gt_u32 s67, 13
	s_cbranch_scc1 .LBB0_1039

; #define PG8_STAGE(bufoff, gbase, voff) do { _Pragma("unroll") for (int _i = 0; _i < 2; ++_i) \
;         __builtin_amdgcn_global_load_lds((const unsigned*)((const char*)(gbase) + (voff)[_i]), (LAS unsigned*)(lds + (bufoff) + ldsw + _i * 8192), 16, 0, 0); } while (0)
; #define PG8_WAIT_V(n) asm volatile("s_waitcnt vmcnt(" #n ")" ::: "memory")
; #define PG8_BAR __builtin_amdgcn_s_barrier()
; template <class Epi, class Sched, bool GATHER, bool F8 = false>
; __device__ __forceinline__ void gemm_phase(LAS unsigned char* lds, const int K, const Sched& S, const Epi& E) {
;     ...
;     if constexpr (EpiInit<Epi>::value) { const typename EpiInit<Epi>::Pre p0 = E.preload(cur, wr, wc, fr, fq); E.init(acc, p0); }
;     int one_scale = 0x7f7f7f7f; asm volatile("" : "+v"(one_scale));
;     bf16x8 At[4][2], B0[2][2], B1[2][2]; i32x8 At8[4], B08[2], B18[2];
;     const char* cA = cur.A; const char* cB = cur.B;
;     PG8_STAGE(PG8_SB(0, 0), cB, voffB); PG8_STAGE(PG8_SB(0, 1), cB + hstepB, voffB); PG8_STAGE(PG8_SA(0, 0), cA, vA[0]); PG8_STAGE(PG8_SA(0, 1), cA, vA[1]);
;     if (wr == 1) PG8_BAR;
;     PG8_WAIT_V(2); PG8_BAR;
;     PG8_STAGE(PG8_SB(1, 0), cB + kstep, voffB); PG8_STAGE(PG8_SA(1, 0), cA + kstep, vA[0]); PG8_STAGE(PG8_SB(1, 1), cB + hstepB + kstep, voffB);
;     PG8_WAIT_V(6); PG8_BAR;
;     __device__ __forceinline__ bool next(int i, Unit& u) const {
;         const int x = c & 7, j = c >> 3, tile = 32 * i + 4 * x + (j & 3), pn = j >> 2;
;         if (tile >= tb.ntiles) return false;
;         const int e = tb.tile_e[tile];
;         u.A = H + (size_t)tile * 256 * DFF; u.B = W + ((size_t)e * DM + pn * 256) * DFF; u.row0 = tile * 256; u.col0 = pn * 256; u.tag = e; u.aux = 0; return true;
;     }
;     __device__ __forceinline__ Pre preload(const Unit& u, int wr, int wc, int fr, int fq) const {
;         const float* pb = bd + (size_t)u.tag * DM + u.col0 + wc * 64 + 8 * fq;
;         Pre p;
; #pragma unroll
;         for (int bj = 0; bj < 2; ++bj)
; #pragma unroll
;             for (int n = 0; n < 2; ++n) p.bv[bj][n] = *(const f32x4*)(pb + bj * 32 + 4 * n);
;         return p;
;     }
.LBB0_1119:
	s_add_i32 s0, 0, 0x20600
	v_mov_b32_e32 v1, s0
	ds_read_b32 v1, v1
	s_lshl_b32 s0, s2, 2
	s_and_b32 s0, s0, 28
	s_bfe_u32 s1, s2, 0x20003
	s_or_b32 s6, s0, s1
	s_waitcnt lgkmcnt(0)
	v_cmp_ge_i32_e32 vcc, s6, v1
	v_readfirstlane_b32 s20, v0
	s_cbranch_vccnz .LBB0_1135
	s_add_u32 s7, s82, 0x34000000
	s_addc_u32 s23, s83, 0
	s_add_u32 s18, s82, 0x24000000
	s_waitcnt vmcnt(0)
	v_lshlrev_b32_e32 v2, 4, v0
	s_addc_u32 s22, s83, 0
	s_lshr_b32 s0, s20, 6
	v_or_b32_e32 v18, 0x2000, v2
	v_and_b32_e32 v5, 32, v0
	s_lshl_b32 s25, s0, 10
	v_lshrrev_b32_e32 v3, 7, v18
	v_bfe_u32 v21, v0, 2, 4
	s_movk_i32 s0, 0x70
	v_bitop3_b32 v19, v2, v5, 48 bitop3:0x6c
	v_and_b32_e32 v20, 64, v0
	v_and_or_b32 v3, v3, s0, v21
	v_or_b32_e32 v2, v19, v20
	v_lshl_or_b32 v146, v3, 11, v2
	v_lshrrev_b32_e32 v3, 5, v0
	v_lshrrev_b32_e32 v6, 1, v0
	v_and_b32_e32 v3, 4, v3
	v_bfe_u32 v5, v0, 2, 2
	v_and_b32_e32 v6, 24, v6
	v_or3_b32 v3, v3, v5, v6
	v_lshrrev_b32_e32 v5, 6, v18
	s_movk_i32 s0, 0xc0
	v_and_or_b32 v5, v5, s0, v3
	s_lshl_b32 s0, s6, 2
	s_add_i32 s0, s0, 0
	s_add_i32 s0, s0, 0x20000
	v_mov_b32_e32 v6, s0
	ds_read_b32 v6, v6
	s_bfe_u32 s16, s20, 0x20006
	s_lshr_b32 s17, s20, 8
	s_lshl_b32 s0, s6, 19
	v_lshrrev_b32_e32 v4, 2, v0
	s_waitcnt lgkmcnt(0)
	v_readfirstlane_b32 s12, v6
	s_ashr_i32 s13, s12, 31
	s_add_u32 s44, s7, s0
	s_addc_u32 s45, s23, 0
	s_lshl_b32 s0, s2, 3
	s_and_b32 s0, s0, 0xffffff00
	s_ashr_i32 s1, s0, 31
	s_lshl_b64 s[2:3], s[12:13], 22
	s_lshl_b64 s[4:5], s[0:1], 11
	s_add_u32 s2, s18, s2
	s_addc_u32 s3, s22, s3
	s_add_u32 s46, s2, s4
	s_addc_u32 s47, s3, s5
	s_lshl_b64 s[2:3], s[12:13], 13
	s_add_u32 s13, s26, s2
	s_addc_u32 s14, s27, s3
	s_lshl_b64 s[2:3], s[0:1], 2
	s_add_u32 s1, s13, s2
	s_addc_u32 s3, s14, s3
	s_lshl_b32 s50, s16, 6
	s_lshl_b32 s2, s16, 8
	s_add_u32 s2, s1, s2
	v_bfe_u32 v22, v0, 4, 2
	v_lshl_or_b32 v150, v5, 11, v2
	v_bfe_u32 v254, v150, 11, 5
	v_and_b32_e32 v150, 0xffff007f, v150
	v_lshl_or_b32 v150, v254, 7, v150
	v_lshrrev_b32_e32 v5, 3, v0
	v_and_or_b32 v3, v4, 64, v3
	s_addc_u32 s3, s3, 0
	s_add_i32 s51, s25, 0
	v_and_or_b32 v5, v5, 48, v21
	v_lshl_or_b32 v156, v3, 11, v2
	v_bfe_u32 v254, v156, 11, 5
	v_and_b32_e32 v156, 0xffff007f, v156
	v_lshl_or_b32 v156, v254, 7, v156
	v_lshlrev_b32_e32 v10, 5, v22
	v_mov_b32_e32 v162, 0x7f7f7f7f
	s_add_i32 m0, s51, 0x10000
	v_lshl_or_b32 v152, v5, 11, v2
	global_load_dwordx4 v[74:77], v10, s[2:3] offset:16
	global_load_dwordx4 v[78:81], v10, s[2:3]
	global_load_dwordx4 v[2:5], v10, s[2:3] offset:144
	global_load_dwordx4 v[6:9], v10, s[2:3] offset:128
	global_load_lds_dwordx4 v156, s[46:47] nt
	s_add_i32 m0, s51, 0x12000
	s_add_u32 s2, s46, 0x10000
	global_load_lds_dwordx4 v150, s[46:47] nt
	s_addc_u32 s3, s47, 0
	s_add_i32 m0, s51, 0x14000
	s_add_i32 s52, s51, 0x2000
	global_load_lds_dwordx4 v156, s[2:3] nt
	s_add_i32 m0, s51, 0x16000
	s_add_i32 s53, s51, 0x4000
	global_load_lds_dwordx4 v150, s[2:3] nt
	s_mov_b32 m0, s51
	v_or_b32_e32 v154, 0x40000, v152
	global_load_lds_dwordx4 v152, s[44:45]
	s_mov_b32 m0, s52
	s_add_i32 s54, s51, 0x6000
	global_load_lds_dwordx4 v146, s[44:45]
	s_mov_b32 m0, s53
	v_or_b32_e32 v148, 0x40000, v146
	global_load_lds_dwordx4 v154, s[44:45]
	s_mov_b32 m0, s54
	v_mov_b32_e32 v157, 0
	global_load_lds_dwordx4 v148, s[44:45]
	v_mov_b32_e32 v151, v157
	v_mov_b32_e32 v153, v157
	v_mov_b32_e32 v147, v157
	s_cmp_eq_u32 s17, 1
	v_lshlrev_b32_e32 v23, 3, v22
	v_lshl_add_u64 v[16:17], s[46:47], 0, v[156:157]
	v_lshl_add_u64 v[14:15], s[46:47], 0, v[150:151]
	v_lshl_add_u64 v[10:11], s[44:45], 0, v[152:153]
	s_cselect_b64 s[2:3], -1, 0
	s_cmp_lg_u32 s17, 1
	v_lshl_add_u64 v[12:13], s[44:45], 0, v[146:147]
	s_cbranch_scc1 .LBB0_1122
	s_barrier
.LBB0_1122:
	s_lshl_b32 s64, s6, 8
	s_add_u32 s14, s82, 0x44600000
	s_addc_u32 s15, s83, 0
	s_lshl_b32 s55, s17, 6
	s_lshl_b32 s1, s17, 13
	s_lshl_b32 s13, s16, 12
	s_mov_b64 s[16:17], 0x80
	s_mov_b64 s[100:101], 0x1000
	s_add_i32 m0, s51, 0x18000
	v_lshl_add_u64 v[16:17], v[16:17], 0, s[100:101]
	s_waitcnt vmcnt(2)
	s_barrier
	global_load_lds_dwordx4 v[16:17], off nt
	v_lshl_add_u64 v[14:15], v[14:15], 0, s[100:101]
	s_add_i32 m0, s51, 0x1a000
	s_add_i32 s56, s51, 0x8000
	s_add_i32 s57, s51, 0xa000
	global_load_lds_dwordx4 v[14:15], off nt
	v_lshl_add_u64 v[10:11], v[10:11], 0, s[16:17]
	s_mov_b32 m0, s56
	s_add_u32 s36, s46, 0x11000
	global_load_lds_dwordx4 v[10:11], off
	v_lshl_add_u64 v[10:11], v[12:13], 0, s[16:17]
	s_mov_b32 m0, s57
	s_addc_u32 s37, s47, 0
	global_load_lds_dwordx4 v[10:11], off
	s_add_i32 m0, s51, 0x1c000
	v_lshl_add_u64 v[10:11], s[36:37], 0, v[156:157]
	global_load_lds_dwordx4 v[10:11], off nt
	v_lshl_add_u64 v[10:11], s[36:37], 0, v[150:151]
	s_add_i32 m0, s51, 0x1e000
	v_lshlrev_b32_e32 v13, 2, v0
	global_load_lds_dwordx4 v[10:11], off nt
	v_and_b32_e32 v10, 15, v0
	v_lshlrev_b32_e32 v11, 4, v22
	v_lshl_or_b32 v12, v10, 6, v11
	v_and_b32_e32 v13, 32, v13
	s_cmpk_lt_u32 s20, 0x100
	v_bitop3_b32 v12, v12, s1, v13 bitop3:0xde
	v_lshlrev_b32_e32 v14, 6, v0
	s_movk_i32 s1, 0x3c0
	s_cselect_b64 s[20:21], -1, 0
	s_add_u32 s58, s18, s4
	v_and_or_b32 v14, v14, s1, v11
	s_addc_u32 s59, s22, s5
	s_add_i32 s4, 0, 0x20800
	v_bitop3_b32 v163, s13, v14, v13 bitop3:0xf6
	v_lshrrev_b32_e32 v13, 6, v0
	s_movk_i32 s5, 0x900
	v_mov_b32_e32 v16, s4
	v_and_b32_e32 v14, 7, v0
	s_movk_i32 s1, 0x90
	v_mad_u32_u24 v13, v13, s5, v16
	v_lshl_or_b32 v164, v14, 3, s50
	v_mad_u32_u24 v10, v10, s1, v13
	v_lshl_add_u32 v13, v14, 4, v13
	v_lshlrev_b32_e32 v14, 8, v0
	v_and_b32_e32 v14, 0x18000, v14
	v_lshlrev_b32_e32 v16, 11, v21
	v_or3_b32 v14, v19, v14, v16
	v_add_u32_e32 v14, v14, v20
	v_or_b32_e32 v158, 0x40000, v14
	v_lshlrev_b32_e32 v14, 4, v18
	v_and_b32_e32 v14, 0x38000, v14
	s_waitcnt vmcnt(6)
	v_bfe_u32 v165, v0, 3, 3
	v_or3_b32 v14, v19, v14, v16
	v_mul_u32_u24_e32 v15, 0x90, v165
	v_add_u32_e32 v14, v14, v20
	v_mov_b32_e32 v155, v157
	v_mov_b32_e32 v149, v157
	s_mov_b32 s19, 0
	v_or_b32_e32 v166, 8, v165
	v_mov_b32_e32 v159, v157
	v_or_b32_e32 v160, 0x40000, v14
	v_mov_b32_e32 v161, v157
	s_mov_b32 s22, 0x42800000
	s_add_i32 s60, 0, 0x10000
	s_add_i32 s61, 0, 0x14000
	v_add_u32_e32 v167, 0, v12
	v_lshlrev_b32_e32 v168, 2, v23
	s_mov_b32 s24, 0x3c800000
	v_add_u32_e32 v169, v10, v11
	v_add_u32_e32 v171, v13, v15
	s_mov_b32 s62, 0
	s_barrier
	s_branch .LBB0_1125

; #define PG8_STAGE(bufoff, gbase, voff) do { _Pragma("unroll") for (int _i = 0; _i < 2; ++_i) \
;         __builtin_amdgcn_global_load_lds((const unsigned*)((const char*)(gbase) + (voff)[_i]), (LAS unsigned*)(lds + (bufoff) + ldsw + _i * 8192), 16, 0, 0); } while (0)
; #define PG8_LDA(dst, b, h) do { _Pragma("unroll") for (int m = 0; m < 4; ++m) { if constexpr (F8) dst##8[m] = PG8_LD32(lds + PG8_SA(b, h) + aoff + m * 2048); \
;         else { _Pragma("unroll") for (int k = 0; k < 2; ++k) dst[m][k] = *(const LAS bf16x8*)(lds + PG8_SA(b, h) + aoff + m * 2048 + k * 1024); } } } while (0)
; #define PG8_LDB(dst, b, h) do { _Pragma("unroll") for (int n = 0; n < 2; ++n) { if constexpr (F8) dst##8[n] = PG8_LD32(lds + PG8_SB(b, h) + boff + n * 2048); \
;         else { _Pragma("unroll") for (int k = 0; k < 2; ++k) dst[n][k] = *(const LAS bf16x8*)(lds + PG8_SB(b, h) + boff + n * 2048 + k * 1024); } } } while (0)
; #define PG8_WAIT_V(n) asm volatile("s_waitcnt vmcnt(" #n ")" ::: "memory")
; #define PG8_WAIT_L(n) asm volatile("s_waitcnt lgkmcnt(" #n ")" ::: "memory")
; #define PG8_BAR __builtin_amdgcn_s_barrier()
; #define PG8_SCHED __builtin_amdgcn_sched_barrier(0)
; template <class Epi, class Sched, bool GATHER, bool F8 = false>
; __device__ __forceinline__ void gemm_phase(LAS unsigned char* lds, const int K, const Sched& S, const Epi& E) {
;     ...
;             PG8_LDB(B0, 0, 0); PG8_LDB(B1, 0, 1); PG8_SCHED; PG8_LDA(At, 0, 0); PG8_STAGE(PG8_SA(1, 1), a1, vA[1]);
;             PG8_WAIT_V(8); PG8_WAIT_L(0); PG8_BAR; PG8_MMA(0, 0, At, B0); PG8_MMA(0, 1, At, B1); PG8_BAR; PG8_SCHED;
;             PG8_LDA(At, 0, 1); PG8_STAGE(PG8_SB(0, 0), b2, voffB); PG8_STAGE(PG8_SB(0, 1), b2 + hstepB, voffB); PG8_STAGE(PG8_SA(0, 0), a2, vN[0]);
;             PG8_WAIT_V(8); PG8_WAIT_L(0); PG8_BAR; PG8_MMA(1, 0, At, B0); PG8_MMA(1, 1, At, B1); PG8_BAR; PG8_SCHED;
.LBB0_1128:
	v_add_u32_e32 v74, s60, v163
	ds_read_b128 v[2:5], v74
	ds_read_b128 v[6:9], v74 offset:1024
	ds_read_b128 v[172:175], v74 offset:2048
	ds_read_b128 v[176:179], v74 offset:3072
	v_add_u32_e32 v74, s61, v163
	ds_read_b128 v[180:183], v74
	ds_read_b128 v[184:187], v74 offset:1024
	ds_read_b128 v[188:191], v74 offset:2048
	ds_read_b128 v[192:195], v74 offset:3072
	s_add_u32 s46, s44, 0x80
	s_addc_u32 s47, s45, 0
	s_cmp_eq_u32 s18, 12
	s_cselect_b32 s49, s41, s47
	s_cselect_b32 s48, s40, s46
	s_cselect_b32 s47, s43, s13
	s_cselect_b32 s46, s42, s1
	v_lshl_add_u64 v[220:221], s[44:45], 0, v[158:159]
	s_add_i32 m0, s51, 0xc000
	ds_read_b128 v[74:77], v167
	ds_read_b128 v[78:81], v167 offset:1024
	ds_read_b128 v[196:199], v167 offset:2048
	ds_read_b128 v[200:203], v167 offset:3072
	ds_read_b128 v[204:207], v167 offset:4096
	ds_read_b128 v[208:211], v167 offset:5120
	ds_read_b128 v[212:215], v167 offset:6144
	ds_read_b128 v[216:219], v167 offset:7168
	global_load_lds_dwordx4 v[220:221], off
	v_lshl_add_u64 v[220:221], s[44:45], 0, v[160:161]
	s_add_i32 m0, s51, 0xe000
	s_nop 0
	global_load_lds_dwordx4 v[220:221], off
	s_waitcnt vmcnt(8)
	s_waitcnt lgkmcnt(0)
	s_barrier
	s_setprio 1
	s_waitcnt lgkmcnt(0)
	v_mfma_scale_f32_16x16x128_f8f6f4 v[142:145], v[2:9], v[74:81], v[142:145], v162, v162 op_sel_hi:[0,0,0]
	v_mfma_scale_f32_16x16x128_f8f6f4 v[138:141], v[172:179], v[74:81], v[138:141], v162, v162 op_sel_hi:[0,0,0]
	v_mfma_scale_f32_16x16x128_f8f6f4 v[126:129], v[2:9], v[196:203], v[126:129], v162, v162 op_sel_hi:[0,0,0]
	v_mfma_scale_f32_16x16x128_f8f6f4 v[122:125], v[172:179], v[196:203], v[122:125], v162, v162 op_sel_hi:[0,0,0]
	v_mfma_scale_f32_16x16x128_f8f6f4 v[110:113], v[2:9], v[204:211], v[110:113], v162, v162 op_sel_hi:[0,0,0]
	v_mfma_scale_f32_16x16x128_f8f6f4 v[106:109], v[172:179], v[204:211], v[106:109], v162, v162 op_sel_hi:[0,0,0]
	v_mfma_scale_f32_16x16x128_f8f6f4 v[94:97], v[2:9], v[212:219], v[94:97], v162, v162 op_sel_hi:[0,0,0]
	v_mfma_scale_f32_16x16x128_f8f6f4 v[90:93], v[172:179], v[212:219], v[90:93], v162, v162 op_sel_hi:[0,0,0]
	s_setprio 0
	s_setprio 1
	v_mfma_scale_f32_16x16x128_f8f6f4 v[134:137], v[180:187], v[74:81], v[134:137], v162, v162 op_sel_hi:[0,0,0]
	v_mfma_scale_f32_16x16x128_f8f6f4 v[130:133], v[188:195], v[74:81], v[130:133], v162, v162 op_sel_hi:[0,0,0]
	v_mfma_scale_f32_16x16x128_f8f6f4 v[118:121], v[180:187], v[196:203], v[118:121], v162, v162 op_sel_hi:[0,0,0]
	v_mfma_scale_f32_16x16x128_f8f6f4 v[114:117], v[188:195], v[196:203], v[114:117], v162, v162 op_sel_hi:[0,0,0]
	v_mfma_scale_f32_16x16x128_f8f6f4 v[102:105], v[180:187], v[204:211], v[102:105], v162, v162 op_sel_hi:[0,0,0]
	v_mfma_scale_f32_16x16x128_f8f6f4 v[98:101], v[188:195], v[204:211], v[98:101], v162, v162 op_sel_hi:[0,0,0]
	v_mfma_scale_f32_16x16x128_f8f6f4 v[86:89], v[180:187], v[212:219], v[86:89], v162, v162 op_sel_hi:[0,0,0]
	v_mfma_scale_f32_16x16x128_f8f6f4 v[82:85], v[188:195], v[212:219], v[82:85], v162, v162 op_sel_hi:[0,0,0]
	s_setprio 0
	s_barrier
	s_add_i32 s65, s60, s25
	v_lshl_add_u64 v[74:75], s[46:47], 0, v[156:157]
	s_mov_b32 m0, s65
	ds_read_b128 v[196:199], v167 offset:16384
	ds_read_b128 v[200:203], v167 offset:17408
	ds_read_b128 v[204:207], v167 offset:18432
	ds_read_b128 v[208:211], v167 offset:19456
	ds_read_b128 v[212:215], v167 offset:20480
	ds_read_b128 v[216:219], v167 offset:21504
	ds_read_b128 v[220:223], v167 offset:22528
	ds_read_b128 v[224:227], v167 offset:23552
	global_load_lds_dwordx4 v[74:75], off nt
	s_add_i32 m0, s65, 0x2000
	s_add_u32 s66, s46, 0x10000
	v_lshl_add_u64 v[76:77], s[46:47], 0, v[150:151]
	s_addc_u32 s67, s47, 0
	s_add_i32 s65, s61, s25
	global_load_lds_dwordx4 v[76:77], off nt
	v_lshl_add_u64 v[78:79], s[66:67], 0, v[156:157]
	s_mov_b32 m0, s65
	v_lshl_add_u64 v[80:81], s[48:49], 0, v[146:147]
	global_load_lds_dwordx4 v[78:79], off nt
	v_lshl_add_u64 v[78:79], s[66:67], 0, v[150:151]
	s_add_i32 m0, s65, 0x2000
	s_nop 0
	global_load_lds_dwordx4 v[78:79], off nt
	v_lshl_add_u64 v[78:79], s[48:49], 0, v[152:153]
	s_mov_b32 m0, s51
	s_nop 0
	global_load_lds_dwordx4 v[78:79], off
	s_mov_b32 m0, s52
	s_nop 0
	global_load_lds_dwordx4 v[80:81], off
	s_waitcnt vmcnt(8)
	s_waitcnt lgkmcnt(0)
	s_barrier
	s_setprio 1
	s_waitcnt lgkmcnt(0)
	v_mfma_scale_f32_16x16x128_f8f6f4 v[70:73], v[2:9], v[196:203], v[70:73], v162, v162 op_sel_hi:[0,0,0]
	v_mfma_scale_f32_16x16x128_f8f6f4 v[66:69], v[172:179], v[196:203], v[66:69], v162, v162 op_sel_hi:[0,0,0]
	v_mfma_scale_f32_16x16x128_f8f6f4 v[54:57], v[2:9], v[204:211], v[54:57], v162, v162 op_sel_hi:[0,0,0]
	v_mfma_scale_f32_16x16x128_f8f6f4 v[50:53], v[172:179], v[204:211], v[50:53], v162, v162 op_sel_hi:[0,0,0]
	v_mfma_scale_f32_16x16x128_f8f6f4 v[38:41], v[2:9], v[212:219], v[38:41], v162, v162 op_sel_hi:[0,0,0]
	v_mfma_scale_f32_16x16x128_f8f6f4 v[34:37], v[172:179], v[212:219], v[34:37], v162, v162 op_sel_hi:[0,0,0]
	v_mfma_scale_f32_16x16x128_f8f6f4 v[18:21], v[2:9], v[220:227], v[18:21], v162, v162 op_sel_hi:[0,0,0]
	v_mfma_scale_f32_16x16x128_f8f6f4 v[22:25], v[172:179], v[220:227], v[22:25], v162, v162 op_sel_hi:[0,0,0]
	s_setprio 0
	s_setprio 1
	v_mfma_scale_f32_16x16x128_f8f6f4 v[62:65], v[180:187], v[196:203], v[62:65], v162, v162 op_sel_hi:[0,0,0]
	v_mfma_scale_f32_16x16x128_f8f6f4 v[58:61], v[188:195], v[196:203], v[58:61], v162, v162 op_sel_hi:[0,0,0]
	v_mfma_scale_f32_16x16x128_f8f6f4 v[46:49], v[180:187], v[204:211], v[46:49], v162, v162 op_sel_hi:[0,0,0]
	v_mfma_scale_f32_16x16x128_f8f6f4 v[42:45], v[188:195], v[204:211], v[42:45], v162, v162 op_sel_hi:[0,0,0]
	v_mfma_scale_f32_16x16x128_f8f6f4 v[30:33], v[180:187], v[212:219], v[30:33], v162, v162 op_sel_hi:[0,0,0]
	v_mfma_scale_f32_16x16x128_f8f6f4 v[26:29], v[188:195], v[212:219], v[26:29], v162, v162 op_sel_hi:[0,0,0]
	v_mfma_scale_f32_16x16x128_f8f6f4 v[10:13], v[180:187], v[220:227], v[10:13], v162, v162 op_sel_hi:[0,0,0]
	v_mfma_scale_f32_16x16x128_f8f6f4 v[14:17], v[188:195], v[220:227], v[14:17], v162, v162 op_sel_hi:[0,0,0]
	s_setprio 0
	s_barrier
; #define PG8_STAGE(bufoff, gbase, voff) do { _Pragma("unroll") for (int _i = 0; _i < 2; ++_i) \
;         __builtin_amdgcn_global_load_lds((const unsigned*)((const char*)(gbase) + (voff)[_i]), (LAS unsigned*)(lds + (bufoff) + ldsw + _i * 8192), 16, 0, 0); } while (0)
; #define PG8_LDA(dst, b, h) do { _Pragma("unroll") for (int m = 0; m < 4; ++m) { if constexpr (F8) dst##8[m] = PG8_LD32(lds + PG8_SA(b, h) + aoff + m * 2048); \
;         else { _Pragma("unroll") for (int k = 0; k < 2; ++k) dst[m][k] = *(const LAS bf16x8*)(lds + PG8_SA(b, h) + aoff + m * 2048 + k * 1024); } } } while (0)
; #define PG8_LDB(dst, b, h) do { _Pragma("unroll") for (int n = 0; n < 2; ++n) { if constexpr (F8) dst##8[n] = PG8_LD32(lds + PG8_SB(b, h) + boff + n * 2048); \
;         else { _Pragma("unroll") for (int k = 0; k < 2; ++k) dst[n][k] = *(const LAS bf16x8*)(lds + PG8_SB(b, h) + boff + n * 2048 + k * 1024); } } } while (0)
; #define PG8_WAIT_V(n) asm volatile("s_waitcnt vmcnt(" #n ")" ::: "memory")
; #define PG8_WAIT_L(n) asm volatile("s_waitcnt lgkmcnt(" #n ")" ::: "memory")
; #define PG8_BAR __builtin_amdgcn_s_barrier()
; #define PG8_SCHED __builtin_amdgcn_sched_barrier(0)
; template <class Epi, class Sched, bool GATHER, bool F8 = false>
; __device__ __forceinline__ void gemm_phase(LAS unsigned char* lds, const int K, const Sched& S, const Epi& E) {
;     ...
;             PG8_LDB(B0, 1, 0); PG8_LDB(B1, 1, 1); PG8_SCHED; PG8_LDA(At, 1, 0); PG8_STAGE(PG8_SA(0, 1), a2, vN[1]);
;             PG8_WAIT_V(8); PG8_WAIT_L(0); PG8_BAR; PG8_MMA(0, 0, At, B0); PG8_MMA(0, 1, At, B1); PG8_BAR; PG8_SCHED;
;             PG8_LDA(At, 1, 1); PG8_STAGE(PG8_SB(1, 0), b3, voffB); PG8_STAGE(PG8_SB(1, 1), b3 + hstepB, voffB); PG8_STAGE(PG8_SA(1, 0), a3, vN[0]);
;             PG8_WAIT_V(8); PG8_WAIT_L(0); PG8_BAR; PG8_MMA(1, 0, At, B0); PG8_MMA(1, 1, At, B1); PG8_BAR; PG8_SCHED;
;         }
;         if (wr == 0) PG8_BAR;
	s_add_i32 s65, 0, 0x18000
	s_add_i32 s66, 0, 0x1c000
	v_add_u32_e32 v2, s65, v163
	v_add_u32_e32 v192, s66, v163
	ds_read_b128 v[172:175], v2
	ds_read_b128 v[176:179], v2 offset:1024
	ds_read_b128 v[180:183], v2 offset:2048
	ds_read_b128 v[184:187], v2 offset:3072
	ds_read_b128 v[2:5], v192
	ds_read_b128 v[6:9], v192 offset:1024
	ds_read_b128 v[188:191], v192 offset:2048
	ds_read_b128 v[192:195], v192 offset:3072
	s_mov_b32 m0, s53
	v_lshl_add_u64 v[228:229], s[48:49], 0, v[154:155]
	ds_read_b128 v[196:199], v167 offset:32768
	ds_read_b128 v[200:203], v167 offset:33792
	ds_read_b128 v[204:207], v167 offset:34816
	ds_read_b128 v[208:211], v167 offset:35840
	ds_read_b128 v[212:215], v167 offset:36864
	ds_read_b128 v[216:219], v167 offset:37888
	ds_read_b128 v[220:223], v167 offset:38912
	ds_read_b128 v[224:227], v167 offset:39936
	global_load_lds_dwordx4 v[228:229], off
	v_lshl_add_u64 v[228:229], s[48:49], 0, v[148:149]
	s_mov_b32 m0, s54
	s_nop 0
	global_load_lds_dwordx4 v[228:229], off
	s_waitcnt vmcnt(8)
	s_waitcnt lgkmcnt(0)
	s_barrier
	s_setprio 1
	s_waitcnt lgkmcnt(0)
	v_mfma_scale_f32_16x16x128_f8f6f4 v[142:145], v[172:179], v[196:203], v[142:145], v162, v162 op_sel_hi:[0,0,0]
	v_mfma_scale_f32_16x16x128_f8f6f4 v[138:141], v[180:187], v[196:203], v[138:141], v162, v162 op_sel_hi:[0,0,0]
	v_mfma_scale_f32_16x16x128_f8f6f4 v[126:129], v[172:179], v[204:211], v[126:129], v162, v162 op_sel_hi:[0,0,0]
	v_mfma_scale_f32_16x16x128_f8f6f4 v[122:125], v[180:187], v[204:211], v[122:125], v162, v162 op_sel_hi:[0,0,0]
	v_mfma_scale_f32_16x16x128_f8f6f4 v[110:113], v[172:179], v[212:219], v[110:113], v162, v162 op_sel_hi:[0,0,0]
	v_mfma_scale_f32_16x16x128_f8f6f4 v[106:109], v[180:187], v[212:219], v[106:109], v162, v162 op_sel_hi:[0,0,0]
	v_mfma_scale_f32_16x16x128_f8f6f4 v[94:97], v[172:179], v[220:227], v[94:97], v162, v162 op_sel_hi:[0,0,0]
	v_mfma_scale_f32_16x16x128_f8f6f4 v[90:93], v[180:187], v[220:227], v[90:93], v162, v162 op_sel_hi:[0,0,0]
	s_setprio 0
	s_setprio 1
	v_mfma_scale_f32_16x16x128_f8f6f4 v[134:137], v[2:9], v[196:203], v[134:137], v162, v162 op_sel_hi:[0,0,0]
	v_mfma_scale_f32_16x16x128_f8f6f4 v[130:133], v[188:195], v[196:203], v[130:133], v162, v162 op_sel_hi:[0,0,0]
	v_mfma_scale_f32_16x16x128_f8f6f4 v[118:121], v[2:9], v[204:211], v[118:121], v162, v162 op_sel_hi:[0,0,0]
	v_mfma_scale_f32_16x16x128_f8f6f4 v[114:117], v[188:195], v[204:211], v[114:117], v162, v162 op_sel_hi:[0,0,0]
	v_mfma_scale_f32_16x16x128_f8f6f4 v[102:105], v[2:9], v[212:219], v[102:105], v162, v162 op_sel_hi:[0,0,0]
	v_mfma_scale_f32_16x16x128_f8f6f4 v[98:101], v[188:195], v[212:219], v[98:101], v162, v162 op_sel_hi:[0,0,0]
	v_mfma_scale_f32_16x16x128_f8f6f4 v[86:89], v[2:9], v[220:227], v[86:89], v162, v162 op_sel_hi:[0,0,0]
	v_mfma_scale_f32_16x16x128_f8f6f4 v[82:85], v[188:195], v[220:227], v[82:85], v162, v162 op_sel_hi:[0,0,0]
	s_setprio 0
	s_barrier
	s_add_i32 s48, s65, s25
	v_lshl_add_u64 v[74:75], v[74:75], 0, s[100:101]
	s_mov_b32 m0, s48
	ds_read_b128 v[196:199], v167 offset:49152
	ds_read_b128 v[200:203], v167 offset:50176
	ds_read_b128 v[204:207], v167 offset:51200
	ds_read_b128 v[208:211], v167 offset:52224
	ds_read_b128 v[212:215], v167 offset:53248
	ds_read_b128 v[216:219], v167 offset:54272
	ds_read_b128 v[220:223], v167 offset:55296
	ds_read_b128 v[224:227], v167 offset:56320
	global_load_lds_dwordx4 v[74:75], off nt
	s_add_i32 m0, s48, 0x2000
	s_add_u32 s46, s46, 0x11000
	v_lshl_add_u64 v[74:75], v[76:77], 0, s[100:101]
	s_addc_u32 s47, s47, 0
	s_add_i32 s48, s66, s25
	global_load_lds_dwordx4 v[74:75], off nt
	v_lshl_add_u64 v[74:75], s[46:47], 0, v[156:157]
	s_mov_b32 m0, s48
	s_nop 0
	global_load_lds_dwordx4 v[74:75], off nt
	v_lshl_add_u64 v[74:75], s[46:47], 0, v[150:151]
	s_add_i32 m0, s48, 0x2000
	s_nop 0
	global_load_lds_dwordx4 v[74:75], off nt
	v_lshl_add_u64 v[74:75], v[78:79], 0, s[16:17]
	s_mov_b32 m0, s56
	s_nop 0
	global_load_lds_dwordx4 v[74:75], off
	v_lshl_add_u64 v[74:75], v[80:81], 0, s[16:17]
	s_mov_b32 m0, s57
	s_nop 0
	global_load_lds_dwordx4 v[74:75], off
	s_waitcnt vmcnt(8)
	s_waitcnt lgkmcnt(0)
	s_barrier
	s_setprio 1
	s_waitcnt lgkmcnt(0)
	v_mfma_scale_f32_16x16x128_f8f6f4 v[70:73], v[172:179], v[196:203], v[70:73], v162, v162 op_sel_hi:[0,0,0]
	v_mfma_scale_f32_16x16x128_f8f6f4 v[66:69], v[180:187], v[196:203], v[66:69], v162, v162 op_sel_hi:[0,0,0]
	v_mfma_scale_f32_16x16x128_f8f6f4 v[54:57], v[172:179], v[204:211], v[54:57], v162, v162 op_sel_hi:[0,0,0]
	v_mfma_scale_f32_16x16x128_f8f6f4 v[50:53], v[180:187], v[204:211], v[50:53], v162, v162 op_sel_hi:[0,0,0]
	v_mfma_scale_f32_16x16x128_f8f6f4 v[38:41], v[172:179], v[212:219], v[38:41], v162, v162 op_sel_hi:[0,0,0]
	v_mfma_scale_f32_16x16x128_f8f6f4 v[34:37], v[180:187], v[212:219], v[34:37], v162, v162 op_sel_hi:[0,0,0]
	v_mfma_scale_f32_16x16x128_f8f6f4 v[18:21], v[172:179], v[220:227], v[18:21], v162, v162 op_sel_hi:[0,0,0]
	v_mfma_scale_f32_16x16x128_f8f6f4 v[22:25], v[180:187], v[220:227], v[22:25], v162, v162 op_sel_hi:[0,0,0]
	s_setprio 0
	s_setprio 1
	v_mfma_scale_f32_16x16x128_f8f6f4 v[62:65], v[2:9], v[196:203], v[62:65], v162, v162 op_sel_hi:[0,0,0]
	v_mfma_scale_f32_16x16x128_f8f6f4 v[58:61], v[188:195], v[196:203], v[58:61], v162, v162 op_sel_hi:[0,0,0]
	v_mfma_scale_f32_16x16x128_f8f6f4 v[46:49], v[2:9], v[204:211], v[46:49], v162, v162 op_sel_hi:[0,0,0]
	v_mfma_scale_f32_16x16x128_f8f6f4 v[42:45], v[188:195], v[204:211], v[42:45], v162, v162 op_sel_hi:[0,0,0]
	v_mfma_scale_f32_16x16x128_f8f6f4 v[30:33], v[2:9], v[212:219], v[30:33], v162, v162 op_sel_hi:[0,0,0]
	v_mfma_scale_f32_16x16x128_f8f6f4 v[26:29], v[188:195], v[212:219], v[26:29], v162, v162 op_sel_hi:[0,0,0]
	v_mfma_scale_f32_16x16x128_f8f6f4 v[10:13], v[2:9], v[220:227], v[10:13], v162, v162 op_sel_hi:[0,0,0]
	v_mfma_scale_f32_16x16x128_f8f6f4 v[14:17], v[188:195], v[220:227], v[14:17], v162, v162 op_sel_hi:[0,0,0]
	s_setprio 0
	s_barrier
	s_add_i32 s18, s18, 2
	s_add_u32 s44, s44, 0x100
	s_addc_u32 s45, s45, 0
	s_add_u32 s1, s1, 0x2000
	s_addc_u32 s13, s13, 0
	s_cmp_gt_u32 s18, 13
	s_cbranch_scc0 .LBB0_1128
	s_and_b64 vcc, exec, s[20:21]
	s_cbranch_vccz .LBB0_1131
	s_barrier
